# v13_epi
# speedup vs baseline: 1.0219x; 1.0219x over previous
.LBB1_65:
	s_or_b64 exec, exec, s[2:3]
	s_waitcnt lgkmcnt(0)
	s_barrier
	ds_read2st64_b32 v[76:77], v223 offset1:2
	v_add_u32_e32 v67, v222, v224
	s_cmp_eq_u64 s[6:7], 0
	s_cbranch_scc0 .Lep1_k1
	v_mov_b32_e32 v18, 0
	v_mov_b32_e32 v19, 0
	v_mov_b32_e32 v20, 0
	v_mov_b32_e32 v21, 0
	ds_read2st64_b32 v[50:51], v221 offset0:0 offset1:1
	ds_read2st64_b32 v[52:53], v221 offset0:2 offset1:3
	ds_read2st64_b32 v[54:55], v221 offset0:4 offset1:5
	ds_read2st64_b32 v[56:57], v221 offset0:6 offset1:7
	ds_read2st64_b32 v[58:59], v221 offset0:8 offset1:9
	ds_read2st64_b32 v[60:61], v221 offset0:10 offset1:11
	ds_read2st64_b32 v[62:63], v67 offset0:0 offset1:2
	ds_read2st64_b32 v[64:65], v67 offset0:4 offset1:6
	ds_read2st64_b32 v[68:69], v67 offset0:16 offset1:18
	ds_read2st64_b32 v[70:71], v67 offset0:20 offset1:22
	ds_read2st64_b32 v[72:73], v67 offset0:32 offset1:34
	ds_read2st64_b32 v[74:75], v67 offset0:36 offset1:38
	s_waitcnt lgkmcnt(12)
	v_fma_f32 v78, -v76, v77, 0
	s_waitcnt lgkmcnt(5)
	v_pk_add_f32 v[34:35], v[34:35], v[50:51]
	v_pk_add_f32 v[34:35], v[34:35], v[78:79] op_sel_hi:[1,0]
	v_pk_fma_f32 v[34:35], v[62:63], v[76:77], v[34:35] op_sel:[0,1,0] op_sel_hi:[1,1,1]
	v_pk_add_f32 v[18:19], v[18:19], v[34:35]
	v_pk_fma_f32 v[20:21], v[34:35], v[34:35], v[20:21]
	s_waitcnt lgkmcnt(4)
	v_pk_add_f32 v[36:37], v[36:37], v[52:53]
	v_pk_add_f32 v[36:37], v[36:37], v[78:79] op_sel_hi:[1,0]
	v_pk_fma_f32 v[36:37], v[64:65], v[76:77], v[36:37] op_sel:[0,1,0] op_sel_hi:[1,1,1]
	v_pk_add_f32 v[18:19], v[18:19], v[36:37]
	v_pk_fma_f32 v[20:21], v[36:37], v[36:37], v[20:21]
	s_waitcnt lgkmcnt(3)
	v_pk_add_f32 v[38:39], v[38:39], v[54:55]
	v_pk_add_f32 v[38:39], v[38:39], v[78:79] op_sel_hi:[1,0]
	v_pk_fma_f32 v[38:39], v[68:69], v[76:77], v[38:39] op_sel:[0,1,0] op_sel_hi:[1,1,1]
	v_pk_add_f32 v[18:19], v[18:19], v[38:39]
	v_pk_fma_f32 v[20:21], v[38:39], v[38:39], v[20:21]
	s_waitcnt lgkmcnt(2)
	v_pk_add_f32 v[40:41], v[40:41], v[56:57]
	v_pk_add_f32 v[40:41], v[40:41], v[78:79] op_sel_hi:[1,0]
	v_pk_fma_f32 v[40:41], v[70:71], v[76:77], v[40:41] op_sel:[0,1,0] op_sel_hi:[1,1,1]
	v_pk_add_f32 v[18:19], v[18:19], v[40:41]
	v_pk_fma_f32 v[20:21], v[40:41], v[40:41], v[20:21]
	s_waitcnt lgkmcnt(1)
	v_pk_add_f32 v[42:43], v[42:43], v[58:59]
	v_pk_add_f32 v[42:43], v[42:43], v[78:79] op_sel_hi:[1,0]
	v_pk_fma_f32 v[42:43], v[72:73], v[76:77], v[42:43] op_sel:[0,1,0] op_sel_hi:[1,1,1]
	v_pk_add_f32 v[18:19], v[18:19], v[42:43]
	v_pk_fma_f32 v[20:21], v[42:43], v[42:43], v[20:21]
	s_waitcnt lgkmcnt(0)
	v_pk_add_f32 v[44:45], v[44:45], v[60:61]
	v_pk_add_f32 v[44:45], v[44:45], v[78:79] op_sel_hi:[1,0]
	v_pk_fma_f32 v[44:45], v[74:75], v[76:77], v[44:45] op_sel:[0,1,0] op_sel_hi:[1,1,1]
	v_pk_add_f32 v[18:19], v[18:19], v[44:45]
	v_pk_fma_f32 v[20:21], v[44:45], v[44:45], v[20:21]
	ds_read2st64_b32 v[50:51], v221 offset0:12 offset1:13
	ds_read2st64_b32 v[52:53], v221 offset0:14 offset1:15
	ds_read2st64_b32 v[54:55], v221 offset0:16 offset1:17
	ds_read2st64_b32 v[56:57], v221 offset0:18 offset1:19
	ds_read2st64_b32 v[58:59], v221 offset0:20 offset1:21
	ds_read2st64_b32 v[60:61], v221 offset0:22 offset1:23
	ds_read2st64_b32 v[62:63], v67 offset0:48 offset1:50
	ds_read2st64_b32 v[64:65], v67 offset0:52 offset1:54
	ds_read2st64_b32 v[68:69], v67 offset0:64 offset1:66
	ds_read2st64_b32 v[70:71], v67 offset0:68 offset1:70
	ds_read2st64_b32 v[72:73], v67 offset0:80 offset1:82
	ds_read2st64_b32 v[74:75], v67 offset0:84 offset1:86
	s_waitcnt lgkmcnt(5)
	v_pk_add_f32 v[46:47], v[46:47], v[50:51]
	v_pk_add_f32 v[46:47], v[46:47], v[78:79] op_sel_hi:[1,0]
	v_pk_fma_f32 v[46:47], v[62:63], v[76:77], v[46:47] op_sel:[0,1,0] op_sel_hi:[1,1,1]
	v_pk_add_f32 v[18:19], v[18:19], v[46:47]
	v_pk_fma_f32 v[20:21], v[46:47], v[46:47], v[20:21]
	s_waitcnt lgkmcnt(4)
	v_pk_add_f32 v[48:49], v[48:49], v[52:53]
	v_pk_add_f32 v[48:49], v[48:49], v[78:79] op_sel_hi:[1,0]
	v_pk_fma_f32 v[48:49], v[64:65], v[76:77], v[48:49] op_sel:[0,1,0] op_sel_hi:[1,1,1]
	v_pk_add_f32 v[18:19], v[18:19], v[48:49]
	v_pk_fma_f32 v[20:21], v[48:49], v[48:49], v[20:21]
	s_waitcnt lgkmcnt(3)
	v_pk_add_f32 v[2:3], v[2:3], v[54:55]
	v_pk_add_f32 v[2:3], v[2:3], v[78:79] op_sel_hi:[1,0]
	v_pk_fma_f32 v[2:3], v[68:69], v[76:77], v[2:3] op_sel:[0,1,0] op_sel_hi:[1,1,1]
	v_pk_add_f32 v[18:19], v[18:19], v[2:3]
	v_pk_fma_f32 v[20:21], v[2:3], v[2:3], v[20:21]
	s_waitcnt lgkmcnt(2)
	v_pk_add_f32 v[4:5], v[4:5], v[56:57]
	v_pk_add_f32 v[4:5], v[4:5], v[78:79] op_sel_hi:[1,0]
	v_pk_fma_f32 v[4:5], v[70:71], v[76:77], v[4:5] op_sel:[0,1,0] op_sel_hi:[1,1,1]
	v_pk_add_f32 v[18:19], v[18:19], v[4:5]
	v_pk_fma_f32 v[20:21], v[4:5], v[4:5], v[20:21]
	s_waitcnt lgkmcnt(1)
	v_pk_add_f32 v[6:7], v[6:7], v[58:59]
	v_pk_add_f32 v[6:7], v[6:7], v[78:79] op_sel_hi:[1,0]
	v_pk_fma_f32 v[6:7], v[72:73], v[76:77], v[6:7] op_sel:[0,1,0] op_sel_hi:[1,1,1]
	v_pk_add_f32 v[18:19], v[18:19], v[6:7]
	v_pk_fma_f32 v[20:21], v[6:7], v[6:7], v[20:21]
	s_waitcnt lgkmcnt(0)
	v_pk_add_f32 v[8:9], v[8:9], v[60:61]
	v_pk_add_f32 v[8:9], v[8:9], v[78:79] op_sel_hi:[1,0]
	v_pk_fma_f32 v[8:9], v[74:75], v[76:77], v[8:9] op_sel:[0,1,0] op_sel_hi:[1,1,1]
	v_pk_add_f32 v[18:19], v[18:19], v[8:9]
	v_pk_fma_f32 v[20:21], v[8:9], v[8:9], v[20:21]
	v_add_f32_e32 v18, v18, v19
	v_add_f32_e32 v20, v20, v21
	v_mov_b32_e32 v19, v18
	v_mov_b32_e32 v21, v20
	s_nop 1
	v_permlane32_swap_b32_e32 v18, v19
	v_permlane32_swap_b32_e32 v20, v21
	v_add_f32_e32 v18, v18, v19
	v_add_f32_e32 v20, v20, v21
	v_cndmask_b32_e64 v22, v20, v18, s[0:1]
	s_branch .Lep1_join
.Lep1_k1:
	v_mov_b32_e32 v34, 0
	v_mov_b32_e32 v35, 0
	v_mov_b32_e32 v36, 0
	v_mov_b32_e32 v37, 0
	ds_read2st64_b32 v[50:51], v221 offset0:24 offset1:25
	ds_read2st64_b32 v[52:53], v221 offset0:26 offset1:27
	ds_read2st64_b32 v[54:55], v221 offset0:28 offset1:29
	ds_read2st64_b32 v[56:57], v221 offset0:30 offset1:31
	ds_read2st64_b32 v[58:59], v221 offset0:32 offset1:33
	ds_read2st64_b32 v[60:61], v221 offset0:34 offset1:35
	ds_read2st64_b32 v[62:63], v67 offset0:96 offset1:98
	ds_read2st64_b32 v[64:65], v67 offset0:100 offset1:102
	ds_read2st64_b32 v[68:69], v67 offset0:112 offset1:114
	ds_read2st64_b32 v[70:71], v67 offset0:116 offset1:118
	ds_read2st64_b32 v[72:73], v67 offset0:128 offset1:130
	ds_read2st64_b32 v[74:75], v67 offset0:132 offset1:134
	s_waitcnt lgkmcnt(12)
	v_fma_f32 v78, -v76, v77, 0
	s_waitcnt lgkmcnt(5)
	v_pk_add_f32 v[10:11], v[10:11], v[50:51]
	v_pk_add_f32 v[10:11], v[10:11], v[78:79] op_sel_hi:[1,0]
	v_pk_fma_f32 v[10:11], v[62:63], v[76:77], v[10:11] op_sel:[0,1,0] op_sel_hi:[1,1,1]
	v_pk_add_f32 v[34:35], v[34:35], v[10:11]
	v_pk_fma_f32 v[36:37], v[10:11], v[10:11], v[36:37]
	s_waitcnt lgkmcnt(4)
	v_pk_add_f32 v[12:13], v[12:13], v[52:53]
	v_pk_add_f32 v[12:13], v[12:13], v[78:79] op_sel_hi:[1,0]
	v_pk_fma_f32 v[12:13], v[64:65], v[76:77], v[12:13] op_sel:[0,1,0] op_sel_hi:[1,1,1]
	v_pk_add_f32 v[34:35], v[34:35], v[12:13]
	v_pk_fma_f32 v[36:37], v[12:13], v[12:13], v[36:37]
	s_waitcnt lgkmcnt(3)
	v_pk_add_f32 v[14:15], v[14:15], v[54:55]
	v_pk_add_f32 v[14:15], v[14:15], v[78:79] op_sel_hi:[1,0]
	v_pk_fma_f32 v[14:15], v[68:69], v[76:77], v[14:15] op_sel:[0,1,0] op_sel_hi:[1,1,1]
	v_pk_add_f32 v[34:35], v[34:35], v[14:15]
	v_pk_fma_f32 v[36:37], v[14:15], v[14:15], v[36:37]
	s_waitcnt lgkmcnt(2)
	v_pk_add_f32 v[16:17], v[16:17], v[56:57]
	v_pk_add_f32 v[16:17], v[16:17], v[78:79] op_sel_hi:[1,0]
	v_pk_fma_f32 v[16:17], v[70:71], v[76:77], v[16:17] op_sel:[0,1,0] op_sel_hi:[1,1,1]
	v_pk_add_f32 v[34:35], v[34:35], v[16:17]
	v_pk_fma_f32 v[36:37], v[16:17], v[16:17], v[36:37]
	s_waitcnt lgkmcnt(1)
	v_pk_add_f32 v[18:19], v[18:19], v[58:59]
	v_pk_add_f32 v[18:19], v[18:19], v[78:79] op_sel_hi:[1,0]
	v_pk_fma_f32 v[18:19], v[72:73], v[76:77], v[18:19] op_sel:[0,1,0] op_sel_hi:[1,1,1]
	v_pk_add_f32 v[34:35], v[34:35], v[18:19]
	v_pk_fma_f32 v[36:37], v[18:19], v[18:19], v[36:37]
	s_waitcnt lgkmcnt(0)
	v_pk_add_f32 v[20:21], v[20:21], v[60:61]
	v_pk_add_f32 v[20:21], v[20:21], v[78:79] op_sel_hi:[1,0]
	v_pk_fma_f32 v[20:21], v[74:75], v[76:77], v[20:21] op_sel:[0,1,0] op_sel_hi:[1,1,1]
	v_pk_add_f32 v[34:35], v[34:35], v[20:21]
	v_pk_fma_f32 v[36:37], v[20:21], v[20:21], v[36:37]
	ds_read2st64_b32 v[50:51], v221 offset0:36 offset1:37
	ds_read2st64_b32 v[52:53], v221 offset0:38 offset1:39
	ds_read2st64_b32 v[62:63], v67 offset0:144 offset1:146
	ds_read2st64_b32 v[64:65], v67 offset0:148 offset1:150
	s_waitcnt lgkmcnt(1)
	v_pk_add_f32 v[22:23], v[22:23], v[50:51]
	v_pk_add_f32 v[22:23], v[22:23], v[78:79] op_sel_hi:[1,0]
	v_pk_fma_f32 v[22:23], v[62:63], v[76:77], v[22:23] op_sel:[0,1,0] op_sel_hi:[1,1,1]
	v_pk_add_f32 v[34:35], v[34:35], v[22:23]
	v_pk_fma_f32 v[36:37], v[22:23], v[22:23], v[36:37]
	s_waitcnt lgkmcnt(0)
	v_pk_add_f32 v[24:25], v[24:25], v[52:53]
	v_pk_add_f32 v[24:25], v[24:25], v[78:79] op_sel_hi:[1,0]
	v_pk_fma_f32 v[24:25], v[64:65], v[76:77], v[24:25] op_sel:[0,1,0] op_sel_hi:[1,1,1]
	v_pk_add_f32 v[34:35], v[34:35], v[24:25]
	v_pk_fma_f32 v[36:37], v[24:25], v[24:25], v[36:37]
	s_mov_b64 s[40:41], exec
	s_and_b64 exec, exec, s[0:1]
	ds_read2st64_b32 v[50:51], v221 offset0:40 offset1:41
	ds_read2st64_b32 v[52:53], v221 offset0:42 offset1:43
	ds_read2st64_b32 v[62:63], v67 offset0:160 offset1:162
	ds_read2st64_b32 v[64:65], v67 offset0:164 offset1:166
	s_waitcnt lgkmcnt(1)
	v_pk_add_f32 v[26:27], v[26:27], v[50:51]
	v_pk_add_f32 v[26:27], v[26:27], v[78:79] op_sel_hi:[1,0]
	v_pk_fma_f32 v[26:27], v[62:63], v[76:77], v[26:27] op_sel:[0,1,0] op_sel_hi:[1,1,1]
	v_pk_add_f32 v[34:35], v[34:35], v[26:27]
	v_pk_fma_f32 v[36:37], v[26:27], v[26:27], v[36:37]
	s_waitcnt lgkmcnt(0)
	v_pk_add_f32 v[28:29], v[28:29], v[52:53]
	v_pk_add_f32 v[28:29], v[28:29], v[78:79] op_sel_hi:[1,0]
	v_pk_fma_f32 v[28:29], v[64:65], v[76:77], v[28:29] op_sel:[0,1,0] op_sel_hi:[1,1,1]
	v_pk_add_f32 v[34:35], v[34:35], v[28:29]
	v_pk_fma_f32 v[36:37], v[28:29], v[28:29], v[36:37]
	s_mov_b64 exec, s[40:41]
	v_add_f32_e32 v34, v34, v35
	v_add_f32_e32 v36, v36, v37
	v_mov_b32_e32 v35, v34
	v_mov_b32_e32 v37, v36
	s_nop 1
	v_permlane32_swap_b32_e32 v34, v35
	v_permlane32_swap_b32_e32 v36, v37
	v_add_f32_e32 v34, v34, v35
	v_add_f32_e32 v36, v36, v37
	v_cndmask_b32_e64 v38, v36, v34, s[0:1]
	ds_write_b32 v236, v38
.Lep1_join:
	s_waitcnt lgkmcnt(0)
	s_barrier
	s_cmp_eq_u64 s[6:7], 0
	s_cbranch_scc0 .Lep1_w1
	ds_read_b32 v50, v236
	v_mul_u32_u24_e32 v51, 37, v1
	v_lshrrev_b32_e32 v51, 8, v51
	v_mul_u32_u24_e32 v52, 7, v51
	v_sub_u32_e32 v52, v1, v52
	v_lshlrev_b32_e32 v53, 6, v51
	v_lshl_add_u32 v53, v52, 3, v53
	v_bfe_u32 v54, v0, 5, 1
	v_lshl_add_u32 v53, v54, 2, v53
	v_lshlrev_b32_e32 v55, 6, v1
	v_add_u32_e32 v55, 0xfffff938, v55
	v_cmp_lt_u32_e32 vcc, 27, v1
	v_readfirstlane_b32 s42, v206
	s_mul_i32 s43, s36, 0x5000
	s_lshr_b32 s40, s67, 8
	s_mul_i32 s40, s40, 0x500
	s_add_i32 s43, s43, s40
	s_mul_i32 s42, s42, 5
	s_add_i32 s43, s43, s42
	s_add_u32 s40, s18, s43
	s_addc_u32 s41, s19, 0
	v_cndmask_b32_e32 v56, v53, v55, vcc
	s_waitcnt lgkmcnt(0)
	v_add_f32_e32 v22, v22, v50
	v_cndmask_b32_e64 v57, v22, 1.0, vcc
	v_mov_b32_e32 v58, v53
	v_mov_b32_e32 v59, v22
	s_movk_i32 s42, 0x138
	v_writelane_b32 v58, s42, 0
	v_writelane_b32 v59, 1.0, 0
	s_mov_b64 s[44:45], exec
	s_mov_b32 exec_lo, -1
	s_mov_b32 exec_hi, 0xfffffff
	global_atomic_add_f32 v56, v57, s[40:41]
	s_mov_b32 exec_lo, 0xf0000001
	s_mov_b32 exec_hi, 0xf0000000
	global_atomic_add_f32 v58, v59, s[40:41]
	s_mov_b64 exec, s[44:45]
	ds_write2st64_b32 v67, v34, v35 offset0:0 offset1:2
	ds_write2st64_b32 v67, v36, v37 offset0:4 offset1:6
	ds_write2st64_b32 v67, v38, v39 offset0:16 offset1:18
	ds_write2st64_b32 v67, v40, v41 offset0:20 offset1:22
	ds_write2st64_b32 v67, v42, v43 offset0:32 offset1:34
	ds_write2st64_b32 v67, v44, v45 offset0:36 offset1:38
	ds_write2st64_b32 v67, v46, v47 offset0:48 offset1:50
	ds_write2st64_b32 v67, v48, v49 offset0:52 offset1:54
	ds_write2st64_b32 v67, v2, v3 offset0:64 offset1:66
	ds_write2st64_b32 v67, v4, v5 offset0:68 offset1:70
	ds_write2st64_b32 v67, v6, v7 offset0:80 offset1:82
	ds_write2st64_b32 v67, v8, v9 offset0:84 offset1:86
	s_branch .Lep1_end
.Lep1_w1:
	ds_write2st64_b32 v67, v10, v11 offset0:96 offset1:98
	ds_write2st64_b32 v67, v12, v13 offset0:100 offset1:102
	ds_write2st64_b32 v67, v14, v15 offset0:112 offset1:114
	ds_write2st64_b32 v67, v16, v17 offset0:116 offset1:118
	ds_write2st64_b32 v67, v18, v19 offset0:128 offset1:130
	ds_write2st64_b32 v67, v20, v21 offset0:132 offset1:134
	ds_write2st64_b32 v67, v22, v23 offset0:144 offset1:146
	ds_write2st64_b32 v67, v24, v25 offset0:148 offset1:150
	s_mov_b64 s[40:41], exec
	s_and_b64 exec, exec, s[0:1]
	ds_write2st64_b32 v67, v26, v27 offset0:160 offset1:162
	ds_write2st64_b32 v67, v28, v29 offset0:164 offset1:166
	s_mov_b64 exec, s[40:41]
.Lep1_end:
	v_mov_b32_e32 v2, v0
	s_waitcnt lgkmcnt(0)
	s_barrier
	s_lshl_b32 s30, s36, 1
	v_ashrrev_i32_e32 v3, 5, v2
	v_lshlrev_b32_e32 v2, 4, v2
	v_and_b32_e32 v2, 0x1f0, v2
	v_min_i32_e32 v4, 0x53, v3
	v_lshl_or_b32 v4, v4, 9, v2
	v_min_i32_e32 v5, 0x43, v3
	v_lshl_or_b32 v5, v5, 9, v2
	ds_read_b128 v[54:57], v4
	ds_read_b128 v[50:53], v5 offset:8192
	v_min_i32_e32 v4, 51, v3
	v_lshl_or_b32 v4, v4, 9, v2
	v_min_i32_e32 v5, 35, v3
	v_lshl_or_b32 v5, v5, 9, v2
	ds_read_b128 v[46:49], v4 offset:16384
	ds_read_b128 v[42:45], v5 offset:24576
	v_min_i32_e32 v4, 19, v3
	v_lshl_or_b32 v4, v4, 9, v2
	v_min_i32_e32 v3, 3, v3
	v_lshl_or_b32 v2, v3, 9, v2
	ds_read_b128 v[38:41], v4 offset:32768
	ds_read_b128 v[34:37], v2 offset:40960
	s_lshl_b64 s[26:27], s[36:37], 17
	v_lshl_add_u64 v[2:3], v[212:213], 0, s[26:27]
	v_add_co_u32_e32 v4, vcc, s65, v2
	global_load_dwordx4 v[100:103], v[2:3], off
	global_load_dwordx4 v[92:95], v[2:3], off offset:1024
	global_load_dwordx4 v[88:91], v[2:3], off offset:2048
	global_load_dwordx4 v[80:83], v[2:3], off offset:3072
	v_addc_co_u32_e32 v5, vcc, 0, v3, vcc
	v_add_co_u32_e32 v6, vcc, s75, v2
	s_lshl_b32 s26, s36, 9
	s_nop 0
	v_addc_co_u32_e32 v7, vcc, 0, v3, vcc
	v_add_co_u32_e32 v2, vcc, s66, v2
	s_mov_b32 s27, s37
	s_nop 0
	v_addc_co_u32_e32 v3, vcc, 0, v3, vcc
	v_lshl_add_u64 v[14:15], s[26:27], 2, v[218:219]
	global_load_dwordx4 v[84:87], v[4:5], off offset:1024
	global_load_dwordx4 v[76:79], v[4:5], off offset:2048
	global_load_dwordx4 v[96:99], v[6:7], off offset:-4096
	global_load_dwordx4 v[128:131], v[6:7], off
	global_load_dwordx4 v[124:127], v[6:7], off offset:1024
	global_load_dwordx4 v[120:123], v[6:7], off offset:2048
	global_load_dwordx4 v[112:115], v[6:7], off offset:3072
	global_load_dwordx4 v[68:71], v[4:5], off offset:3072
	global_load_dwordx4 v[116:119], v[2:3], off
	global_load_dwordx4 v[108:111], v[2:3], off offset:1024
	global_load_dwordx4 v[104:107], v[2:3], off offset:2048
	global_load_dwordx4 v[72:75], v[2:3], off offset:3072
	global_load_dwordx4 v[18:21], v[14:15], off offset:1536
	global_load_dwordx4 v[22:25], v[14:15], off offset:1568
	s_nop 0
	global_load_dwordx4 v[2:5], v[14:15], off offset:1664
	global_load_dwordx4 v[6:9], v[14:15], off offset:1696
	global_load_dwordx4 v[26:29], v[14:15], off offset:1600
	global_load_dwordx4 v[30:33], v[14:15], off offset:1632
	global_load_dwordx4 v[10:13], v[14:15], off offset:1728
	s_nop 0
	global_load_dwordx4 v[14:17], v[14:15], off offset:1760
	v_mov_b32_e32 v58, v0
	s_or_b32 s80, s30, 1
	s_lshl_b32 s26, s36, 7
	s_nop 0
	v_cmp_gt_i32_e32 vcc, s76, v58
	s_and_saveexec_b64 s[30:31], vcc
	s_cbranch_execz .LBB1_126
	s_lshl_b64 s[40:41], s[26:27], 2
	s_add_u32 s40, s22, s40
	s_addc_u32 s41, s23, s41
	v_and_b32_e32 v58, 63, v0
	v_lshrrev_b32_e32 v64, 6, v0
	v_lshrrev_b32_e32 v59, 3, v58
	v_and_b32_e32 v60, 7, v58
	v_readfirstlane_b32 s52, v64
	v_min_u32_e32 v61, 4, v59
	v_lshlrev_b32_e32 v62, 6, v61
	v_lshl_add_u32 v62, v60, 3, v62
	v_mul_u32_u24_e32 v63, 7, v61
	v_add_u32_e32 v63, v63, v60
	v_cmp_gt_u32_e64 s[46:47], 5, v59
	v_cmp_gt_u32_e64 s[48:49], 7, v60
	v_cmp_gt_u32_e32 vcc, 32, v63
	v_cmp_eq_u32_e64 s[50:51], 7, v60
	s_and_b64 s[46:47], s[46:47], s[48:49]
	s_and_b64 s[46:47], s[46:47], vcc
	v_min_u32_e32 v63, 31, v63
	v_lshl_add_u32 v63, v64, 5, v63
	v_lshlrev_b32_e32 v65, 2, v63
	global_load_dword v132, v65, s[40:41]
	v_lshl_add_u32 v133, v63, 2, v249
	s_mul_i32 s52, s52, 0x140
	s_mul_i32 s53, s36, 0x5000
	s_add_i32 s53, s53, s52
	s_add_u32 s42, s18, s53
	s_addc_u32 s43, s19, 0
	s_add_u32 s44, s42, 0x1400
	s_addc_u32 s45, s43, 0
	s_mov_b32 s82, 0x10000
	s_mov_b32 s81, 0x43800000

.LBB1_146:
	s_or_b64 exec, exec, s[2:3]
	s_waitcnt lgkmcnt(0)
	s_barrier
	ds_read2st64_b32 v[76:77], v223 offset1:2
	v_add_u32_e32 v67, v222, v224
	s_cmp_eq_u64 s[6:7], 0
	s_cbranch_scc0 .Lep2_k1
	v_mov_b32_e32 v18, 0
	v_mov_b32_e32 v19, 0
	v_mov_b32_e32 v20, 0
	v_mov_b32_e32 v21, 0
	ds_read2st64_b32 v[50:51], v221 offset0:0 offset1:1
	ds_read2st64_b32 v[52:53], v221 offset0:2 offset1:3
	ds_read2st64_b32 v[54:55], v221 offset0:4 offset1:5
	ds_read2st64_b32 v[56:57], v221 offset0:6 offset1:7
	ds_read2st64_b32 v[58:59], v221 offset0:8 offset1:9
	ds_read2st64_b32 v[60:61], v221 offset0:10 offset1:11
	ds_read2st64_b32 v[62:63], v67 offset0:0 offset1:2
	ds_read2st64_b32 v[64:65], v67 offset0:4 offset1:6
	ds_read2st64_b32 v[68:69], v67 offset0:16 offset1:18
	ds_read2st64_b32 v[70:71], v67 offset0:20 offset1:22
	ds_read2st64_b32 v[72:73], v67 offset0:32 offset1:34
	ds_read2st64_b32 v[74:75], v67 offset0:36 offset1:38
	s_waitcnt lgkmcnt(12)
	v_fma_f32 v78, -v76, v77, v173
	s_waitcnt lgkmcnt(5)
	v_pk_add_f32 v[34:35], v[34:35], v[50:51]
	v_pk_add_f32 v[34:35], v[34:35], v[78:79] op_sel_hi:[1,0]
	v_pk_fma_f32 v[34:35], v[62:63], v[76:77], v[34:35] op_sel:[0,1,0] op_sel_hi:[1,1,1]
	v_pk_add_f32 v[18:19], v[18:19], v[34:35]
	v_pk_fma_f32 v[20:21], v[34:35], v[34:35], v[20:21]
	s_waitcnt lgkmcnt(4)
	v_pk_add_f32 v[36:37], v[36:37], v[52:53]
	v_pk_add_f32 v[36:37], v[36:37], v[78:79] op_sel_hi:[1,0]
	v_pk_fma_f32 v[36:37], v[64:65], v[76:77], v[36:37] op_sel:[0,1,0] op_sel_hi:[1,1,1]
	v_pk_add_f32 v[18:19], v[18:19], v[36:37]
	v_pk_fma_f32 v[20:21], v[36:37], v[36:37], v[20:21]
	s_waitcnt lgkmcnt(3)
	v_pk_add_f32 v[38:39], v[38:39], v[54:55]
	v_pk_add_f32 v[38:39], v[38:39], v[78:79] op_sel_hi:[1,0]
	v_pk_fma_f32 v[38:39], v[68:69], v[76:77], v[38:39] op_sel:[0,1,0] op_sel_hi:[1,1,1]
	v_pk_add_f32 v[18:19], v[18:19], v[38:39]
	v_pk_fma_f32 v[20:21], v[38:39], v[38:39], v[20:21]
	s_waitcnt lgkmcnt(2)
	v_pk_add_f32 v[40:41], v[40:41], v[56:57]
	v_pk_add_f32 v[40:41], v[40:41], v[78:79] op_sel_hi:[1,0]
	v_pk_fma_f32 v[40:41], v[70:71], v[76:77], v[40:41] op_sel:[0,1,0] op_sel_hi:[1,1,1]
	v_pk_add_f32 v[18:19], v[18:19], v[40:41]
	v_pk_fma_f32 v[20:21], v[40:41], v[40:41], v[20:21]
	s_waitcnt lgkmcnt(1)
	v_pk_add_f32 v[42:43], v[42:43], v[58:59]
	v_pk_add_f32 v[42:43], v[42:43], v[78:79] op_sel_hi:[1,0]
	v_pk_fma_f32 v[42:43], v[72:73], v[76:77], v[42:43] op_sel:[0,1,0] op_sel_hi:[1,1,1]
	v_pk_add_f32 v[18:19], v[18:19], v[42:43]
	v_pk_fma_f32 v[20:21], v[42:43], v[42:43], v[20:21]
	s_waitcnt lgkmcnt(0)
	v_pk_add_f32 v[44:45], v[44:45], v[60:61]
	v_pk_add_f32 v[44:45], v[44:45], v[78:79] op_sel_hi:[1,0]
	v_pk_fma_f32 v[44:45], v[74:75], v[76:77], v[44:45] op_sel:[0,1,0] op_sel_hi:[1,1,1]
	v_pk_add_f32 v[18:19], v[18:19], v[44:45]
	v_pk_fma_f32 v[20:21], v[44:45], v[44:45], v[20:21]
	ds_read2st64_b32 v[50:51], v221 offset0:12 offset1:13
	ds_read2st64_b32 v[52:53], v221 offset0:14 offset1:15
	ds_read2st64_b32 v[54:55], v221 offset0:16 offset1:17
	ds_read2st64_b32 v[56:57], v221 offset0:18 offset1:19
	ds_read2st64_b32 v[58:59], v221 offset0:20 offset1:21
	ds_read2st64_b32 v[60:61], v221 offset0:22 offset1:23
	ds_read2st64_b32 v[62:63], v67 offset0:48 offset1:50
	ds_read2st64_b32 v[64:65], v67 offset0:52 offset1:54
	ds_read2st64_b32 v[68:69], v67 offset0:64 offset1:66
	ds_read2st64_b32 v[70:71], v67 offset0:68 offset1:70
	ds_read2st64_b32 v[72:73], v67 offset0:80 offset1:82
	ds_read2st64_b32 v[74:75], v67 offset0:84 offset1:86
	s_waitcnt lgkmcnt(5)
	v_pk_add_f32 v[46:47], v[46:47], v[50:51]
	v_pk_add_f32 v[46:47], v[46:47], v[78:79] op_sel_hi:[1,0]
	v_pk_fma_f32 v[46:47], v[62:63], v[76:77], v[46:47] op_sel:[0,1,0] op_sel_hi:[1,1,1]
	v_pk_add_f32 v[18:19], v[18:19], v[46:47]
	v_pk_fma_f32 v[20:21], v[46:47], v[46:47], v[20:21]
	s_waitcnt lgkmcnt(4)
	v_pk_add_f32 v[48:49], v[48:49], v[52:53]
	v_pk_add_f32 v[48:49], v[48:49], v[78:79] op_sel_hi:[1,0]
	v_pk_fma_f32 v[48:49], v[64:65], v[76:77], v[48:49] op_sel:[0,1,0] op_sel_hi:[1,1,1]
	v_pk_add_f32 v[18:19], v[18:19], v[48:49]
	v_pk_fma_f32 v[20:21], v[48:49], v[48:49], v[20:21]
	s_waitcnt lgkmcnt(3)
	v_pk_add_f32 v[2:3], v[2:3], v[54:55]
	v_pk_add_f32 v[2:3], v[2:3], v[78:79] op_sel_hi:[1,0]
	v_pk_fma_f32 v[2:3], v[68:69], v[76:77], v[2:3] op_sel:[0,1,0] op_sel_hi:[1,1,1]
	v_pk_add_f32 v[18:19], v[18:19], v[2:3]
	v_pk_fma_f32 v[20:21], v[2:3], v[2:3], v[20:21]
	s_waitcnt lgkmcnt(2)
	v_pk_add_f32 v[4:5], v[4:5], v[56:57]
	v_pk_add_f32 v[4:5], v[4:5], v[78:79] op_sel_hi:[1,0]
	v_pk_fma_f32 v[4:5], v[70:71], v[76:77], v[4:5] op_sel:[0,1,0] op_sel_hi:[1,1,1]
	v_pk_add_f32 v[18:19], v[18:19], v[4:5]
	v_pk_fma_f32 v[20:21], v[4:5], v[4:5], v[20:21]
	s_waitcnt lgkmcnt(1)
	v_pk_add_f32 v[6:7], v[6:7], v[58:59]
	v_pk_add_f32 v[6:7], v[6:7], v[78:79] op_sel_hi:[1,0]
	v_pk_fma_f32 v[6:7], v[72:73], v[76:77], v[6:7] op_sel:[0,1,0] op_sel_hi:[1,1,1]
	v_pk_add_f32 v[18:19], v[18:19], v[6:7]
	v_pk_fma_f32 v[20:21], v[6:7], v[6:7], v[20:21]
	s_waitcnt lgkmcnt(0)
	v_pk_add_f32 v[8:9], v[8:9], v[60:61]
	v_pk_add_f32 v[8:9], v[8:9], v[78:79] op_sel_hi:[1,0]
	v_pk_fma_f32 v[8:9], v[74:75], v[76:77], v[8:9] op_sel:[0,1,0] op_sel_hi:[1,1,1]
	v_pk_add_f32 v[18:19], v[18:19], v[8:9]
	v_pk_fma_f32 v[20:21], v[8:9], v[8:9], v[20:21]
	v_add_f32_e32 v18, v18, v19
	v_add_f32_e32 v20, v20, v21
	v_mov_b32_e32 v19, v18
	v_mov_b32_e32 v21, v20
	s_nop 1
	v_permlane32_swap_b32_e32 v18, v19
	v_permlane32_swap_b32_e32 v20, v21
	v_add_f32_e32 v18, v18, v19
	v_add_f32_e32 v20, v20, v21
	v_cndmask_b32_e64 v22, v20, v18, s[0:1]
	s_branch .Lep2_join
.Lep2_k1:
	v_mov_b32_e32 v34, 0
	v_mov_b32_e32 v35, 0
	v_mov_b32_e32 v36, 0
	v_mov_b32_e32 v37, 0
	ds_read2st64_b32 v[50:51], v221 offset0:24 offset1:25
	ds_read2st64_b32 v[52:53], v221 offset0:26 offset1:27
	ds_read2st64_b32 v[54:55], v221 offset0:28 offset1:29
	ds_read2st64_b32 v[56:57], v221 offset0:30 offset1:31
	ds_read2st64_b32 v[58:59], v221 offset0:32 offset1:33
	ds_read2st64_b32 v[60:61], v221 offset0:34 offset1:35
	ds_read2st64_b32 v[62:63], v67 offset0:96 offset1:98
	ds_read2st64_b32 v[64:65], v67 offset0:100 offset1:102
	ds_read2st64_b32 v[68:69], v67 offset0:112 offset1:114
	ds_read2st64_b32 v[70:71], v67 offset0:116 offset1:118
	ds_read2st64_b32 v[72:73], v67 offset0:128 offset1:130
	ds_read2st64_b32 v[74:75], v67 offset0:132 offset1:134
	s_waitcnt lgkmcnt(12)
	v_fma_f32 v78, -v76, v77, v173
	s_waitcnt lgkmcnt(5)
	v_pk_add_f32 v[10:11], v[10:11], v[50:51]
	v_pk_add_f32 v[10:11], v[10:11], v[78:79] op_sel_hi:[1,0]
	v_pk_fma_f32 v[10:11], v[62:63], v[76:77], v[10:11] op_sel:[0,1,0] op_sel_hi:[1,1,1]
	v_pk_add_f32 v[34:35], v[34:35], v[10:11]
	v_pk_fma_f32 v[36:37], v[10:11], v[10:11], v[36:37]
	s_waitcnt lgkmcnt(4)
	v_pk_add_f32 v[12:13], v[12:13], v[52:53]
	v_pk_add_f32 v[12:13], v[12:13], v[78:79] op_sel_hi:[1,0]
	v_pk_fma_f32 v[12:13], v[64:65], v[76:77], v[12:13] op_sel:[0,1,0] op_sel_hi:[1,1,1]
	v_pk_add_f32 v[34:35], v[34:35], v[12:13]
	v_pk_fma_f32 v[36:37], v[12:13], v[12:13], v[36:37]
	s_waitcnt lgkmcnt(3)
	v_pk_add_f32 v[14:15], v[14:15], v[54:55]
	v_pk_add_f32 v[14:15], v[14:15], v[78:79] op_sel_hi:[1,0]
	v_pk_fma_f32 v[14:15], v[68:69], v[76:77], v[14:15] op_sel:[0,1,0] op_sel_hi:[1,1,1]
	v_pk_add_f32 v[34:35], v[34:35], v[14:15]
	v_pk_fma_f32 v[36:37], v[14:15], v[14:15], v[36:37]
	s_waitcnt lgkmcnt(2)
	v_pk_add_f32 v[16:17], v[16:17], v[56:57]
	v_pk_add_f32 v[16:17], v[16:17], v[78:79] op_sel_hi:[1,0]
	v_pk_fma_f32 v[16:17], v[70:71], v[76:77], v[16:17] op_sel:[0,1,0] op_sel_hi:[1,1,1]
	v_pk_add_f32 v[34:35], v[34:35], v[16:17]
	v_pk_fma_f32 v[36:37], v[16:17], v[16:17], v[36:37]
	s_waitcnt lgkmcnt(1)
	v_pk_add_f32 v[18:19], v[18:19], v[58:59]
	v_pk_add_f32 v[18:19], v[18:19], v[78:79] op_sel_hi:[1,0]
	v_pk_fma_f32 v[18:19], v[72:73], v[76:77], v[18:19] op_sel:[0,1,0] op_sel_hi:[1,1,1]
	v_pk_add_f32 v[34:35], v[34:35], v[18:19]
	v_pk_fma_f32 v[36:37], v[18:19], v[18:19], v[36:37]
	s_waitcnt lgkmcnt(0)
	v_pk_add_f32 v[20:21], v[20:21], v[60:61]
	v_pk_add_f32 v[20:21], v[20:21], v[78:79] op_sel_hi:[1,0]
	v_pk_fma_f32 v[20:21], v[74:75], v[76:77], v[20:21] op_sel:[0,1,0] op_sel_hi:[1,1,1]
	v_pk_add_f32 v[34:35], v[34:35], v[20:21]
	v_pk_fma_f32 v[36:37], v[20:21], v[20:21], v[36:37]
	ds_read2st64_b32 v[50:51], v221 offset0:36 offset1:37
	ds_read2st64_b32 v[52:53], v221 offset0:38 offset1:39
	ds_read2st64_b32 v[62:63], v67 offset0:144 offset1:146
	ds_read2st64_b32 v[64:65], v67 offset0:148 offset1:150
	s_waitcnt lgkmcnt(1)
	v_pk_add_f32 v[22:23], v[22:23], v[50:51]
	v_pk_add_f32 v[22:23], v[22:23], v[78:79] op_sel_hi:[1,0]
	v_pk_fma_f32 v[22:23], v[62:63], v[76:77], v[22:23] op_sel:[0,1,0] op_sel_hi:[1,1,1]
	v_pk_add_f32 v[34:35], v[34:35], v[22:23]
	v_pk_fma_f32 v[36:37], v[22:23], v[22:23], v[36:37]
	s_waitcnt lgkmcnt(0)
	v_pk_add_f32 v[24:25], v[24:25], v[52:53]
	v_pk_add_f32 v[24:25], v[24:25], v[78:79] op_sel_hi:[1,0]
	v_pk_fma_f32 v[24:25], v[64:65], v[76:77], v[24:25] op_sel:[0,1,0] op_sel_hi:[1,1,1]
	v_pk_add_f32 v[34:35], v[34:35], v[24:25]
	v_pk_fma_f32 v[36:37], v[24:25], v[24:25], v[36:37]
	s_mov_b64 s[40:41], exec
	s_and_b64 exec, exec, s[0:1]
	ds_read2st64_b32 v[50:51], v221 offset0:40 offset1:41
	ds_read2st64_b32 v[52:53], v221 offset0:42 offset1:43
	ds_read2st64_b32 v[62:63], v67 offset0:160 offset1:162
	ds_read2st64_b32 v[64:65], v67 offset0:164 offset1:166
	s_waitcnt lgkmcnt(1)
	v_pk_add_f32 v[26:27], v[26:27], v[50:51]
	v_pk_add_f32 v[26:27], v[26:27], v[78:79] op_sel_hi:[1,0]
	v_pk_fma_f32 v[26:27], v[62:63], v[76:77], v[26:27] op_sel:[0,1,0] op_sel_hi:[1,1,1]
	v_pk_add_f32 v[34:35], v[34:35], v[26:27]
	v_pk_fma_f32 v[36:37], v[26:27], v[26:27], v[36:37]
	s_waitcnt lgkmcnt(0)
	v_pk_add_f32 v[28:29], v[28:29], v[52:53]
	v_pk_add_f32 v[28:29], v[28:29], v[78:79] op_sel_hi:[1,0]
	v_pk_fma_f32 v[28:29], v[64:65], v[76:77], v[28:29] op_sel:[0,1,0] op_sel_hi:[1,1,1]
	v_pk_add_f32 v[34:35], v[34:35], v[28:29]
	v_pk_fma_f32 v[36:37], v[28:29], v[28:29], v[36:37]
	s_mov_b64 exec, s[40:41]
	v_add_f32_e32 v34, v34, v35
	v_add_f32_e32 v36, v36, v37
	v_mov_b32_e32 v35, v34
	v_mov_b32_e32 v37, v36
	s_nop 1
	v_permlane32_swap_b32_e32 v34, v35
	v_permlane32_swap_b32_e32 v36, v37
	v_add_f32_e32 v34, v34, v35
	v_add_f32_e32 v36, v36, v37
	v_cndmask_b32_e64 v38, v36, v34, s[0:1]
	ds_write_b32 v236, v38
.Lep2_join:
	s_waitcnt lgkmcnt(0)
	s_barrier
	s_cmp_eq_u64 s[6:7], 0
	s_cbranch_scc0 .Lep2_w1
	ds_read_b32 v50, v236
	v_mul_u32_u24_e32 v51, 37, v1
	v_lshrrev_b32_e32 v51, 8, v51
	v_mul_u32_u24_e32 v52, 7, v51
	v_sub_u32_e32 v52, v1, v52
	v_lshlrev_b32_e32 v53, 6, v51
	v_lshl_add_u32 v53, v52, 3, v53
	v_bfe_u32 v54, v0, 5, 1
	v_lshl_add_u32 v53, v54, 2, v53
	v_lshlrev_b32_e32 v55, 6, v1
	v_add_u32_e32 v55, 0xfffff938, v55
	v_cmp_lt_u32_e32 vcc, 27, v1
	v_readfirstlane_b32 s42, v206
	s_mul_i32 s43, s36, 0x5000
	s_addk_i32 s43, 0x2800
	s_lshr_b32 s40, s67, 8
	s_mul_i32 s40, s40, 0x500
	s_add_i32 s43, s43, s40
	s_mul_i32 s42, s42, 5
	s_add_i32 s43, s43, s42
	s_add_u32 s40, s18, s43
	s_addc_u32 s41, s19, 0
	v_cndmask_b32_e32 v56, v53, v55, vcc
	s_waitcnt lgkmcnt(0)
	v_add_f32_e32 v22, v22, v50
	v_cndmask_b32_e64 v57, v22, 1.0, vcc
	v_mov_b32_e32 v58, v53
	v_mov_b32_e32 v59, v22
	s_movk_i32 s42, 0x138
	v_writelane_b32 v58, s42, 0
	v_writelane_b32 v59, 1.0, 0
	s_mov_b64 s[44:45], exec
	s_mov_b32 exec_lo, -1
	s_mov_b32 exec_hi, 0xfffffff
	global_atomic_add_f32 v56, v57, s[40:41]
	s_mov_b32 exec_lo, 0xf0000001
	s_mov_b32 exec_hi, 0xf0000000
	global_atomic_add_f32 v58, v59, s[40:41]
	s_mov_b64 exec, s[44:45]
	ds_write2st64_b32 v67, v34, v35 offset0:0 offset1:2
	ds_write2st64_b32 v67, v36, v37 offset0:4 offset1:6
	ds_write2st64_b32 v67, v38, v39 offset0:16 offset1:18
	ds_write2st64_b32 v67, v40, v41 offset0:20 offset1:22
	ds_write2st64_b32 v67, v42, v43 offset0:32 offset1:34
	ds_write2st64_b32 v67, v44, v45 offset0:36 offset1:38
	ds_write2st64_b32 v67, v46, v47 offset0:48 offset1:50
	ds_write2st64_b32 v67, v48, v49 offset0:52 offset1:54
	ds_write2st64_b32 v67, v2, v3 offset0:64 offset1:66
	ds_write2st64_b32 v67, v4, v5 offset0:68 offset1:70
	ds_write2st64_b32 v67, v6, v7 offset0:80 offset1:82
	ds_write2st64_b32 v67, v8, v9 offset0:84 offset1:86
	s_branch .Lep2_end

.Lep2_end:
	v_mov_b32_e32 v2, v0
	s_waitcnt lgkmcnt(0)
	s_barrier
	s_nop 0
	v_ashrrev_i32_e32 v3, 5, v2
	v_lshlrev_b32_e32 v2, 4, v2
	v_and_b32_e32 v2, 0x1f0, v2
	v_min_i32_e32 v4, 0x53, v3
	v_lshl_or_b32 v4, v4, 9, v2
	v_min_i32_e32 v5, 0x43, v3
	v_lshl_or_b32 v5, v5, 9, v2
	ds_read_b128 v[42:45], v4
	ds_read_b128 v[38:41], v5 offset:8192
	v_min_i32_e32 v4, 51, v3
	v_lshl_or_b32 v4, v4, 9, v2
	v_min_i32_e32 v5, 35, v3
	v_lshl_or_b32 v5, v5, 9, v2
	ds_read_b128 v[34:37], v4 offset:16384
	ds_read_b128 v[30:33], v5 offset:24576
	v_min_i32_e32 v4, 19, v3
	v_lshl_or_b32 v4, v4, 9, v2
	v_min_i32_e32 v3, 3, v3
	v_lshl_or_b32 v2, v3, 9, v2
	ds_read_b128 v[22:25], v4 offset:32768
	ds_read_b128 v[18:21], v2 offset:40960
	s_add_i32 s80, s36, 1
	s_cmp_lg_u32 s36, 2
	s_cselect_b64 s[30:31], -1, 0
	s_and_b64 s[40:41], s[30:31], exec
	s_cselect_b32 s42, s80, 2
	s_lshl_b32 s40, s42, 15
	s_mov_b32 s41, s37
	v_lshl_add_u64 v[2:3], v[196:197], 0, s[40:41]
	v_lshl_add_u64 v[4:5], v[198:199], 0, s[40:41]
	v_lshl_add_u64 v[6:7], v[200:201], 0, s[40:41]
	global_load_dwordx4 v[116:119], v[2:3], off
	global_load_dwordx4 v[120:123], v[2:3], off offset:1024
	global_load_dwordx4 v[112:115], v[4:5], off
	global_load_dwordx4 v[100:103], v[4:5], off offset:1024
	global_load_dwordx4 v[96:99], v[6:7], off
	global_load_dwordx4 v[76:79], v[6:7], off offset:1024
	global_load_dwordx4 v[124:127], v[2:3], off offset:2048
	global_load_dwordx4 v[128:131], v[2:3], off offset:3072
	global_load_dwordx4 v[104:107], v[4:5], off offset:2048
	global_load_dwordx4 v[108:111], v[4:5], off offset:3072
	global_load_dwordx4 v[72:75], v[6:7], off offset:2048
	global_load_dwordx4 v[68:71], v[6:7], off offset:3072
	v_add_co_u32_e32 v2, vcc, s65, v2
	s_lshl_b32 s40, s42, 7
	s_nop 0
	v_addc_co_u32_e32 v3, vcc, 0, v3, vcc
	v_add_co_u32_e32 v4, vcc, s65, v4
	v_lshl_add_u64 v[14:15], s[40:41], 2, v[202:203]
	s_nop 0
	v_addc_co_u32_e32 v5, vcc, 0, v5, vcc
	v_add_co_u32_e32 v6, vcc, s65, v6
	s_nop 1
	v_addc_co_u32_e32 v7, vcc, 0, v7, vcc
	global_load_dwordx4 v[148:151], v[2:3], off
	global_load_dwordx4 v[152:155], v[2:3], off offset:1024
	global_load_dwordx4 v[132:135], v[4:5], off
	global_load_dwordx4 v[136:139], v[4:5], off offset:1024
	global_load_dwordx4 v[92:95], v[6:7], off
	global_load_dwordx4 v[84:87], v[6:7], off offset:1024
	global_load_dwordx4 v[156:159], v[2:3], off offset:2048
	global_load_dwordx4 v[160:163], v[2:3], off offset:3072
	global_load_dwordx4 v[140:143], v[4:5], off offset:2048
	global_load_dwordx4 v[144:147], v[4:5], off offset:3072
	global_load_dwordx4 v[88:91], v[6:7], off offset:2048
	global_load_dwordx4 v[80:83], v[6:7], off offset:3072
	s_nop 0
	global_load_dwordx4 v[2:5], v[14:15], off
	global_load_dwordx4 v[6:9], v[14:15], off offset:32
	global_load_dwordx4 v[10:13], v[14:15], off offset:64
	s_nop 0
	global_load_dwordx4 v[14:17], v[14:15], off offset:96
	s_nop 0
	global_load_dwordx4 v[26:29], v[216:217], off offset:1024
	v_mov_b32_e32 v46, v0
	s_nop 0
	v_cmp_gt_i32_e32 vcc, s76, v46
	s_and_saveexec_b64 s[40:41], vcc
	s_cbranch_execz .LBB1_207
	s_lshl_b64 s[26:27], s[26:27], 2
	s_add_u32 s26, s24, s26
	s_addc_u32 s27, s25, s27
	v_and_b32_e32 v46, 63, v0
	v_lshrrev_b32_e32 v52, 6, v0
	v_lshrrev_b32_e32 v47, 3, v46
	v_and_b32_e32 v48, 7, v46
	v_readfirstlane_b32 s52, v52
	v_min_u32_e32 v49, 4, v47
	v_lshlrev_b32_e32 v50, 6, v49
	v_lshl_add_u32 v50, v48, 3, v50
	v_mul_u32_u24_e32 v51, 7, v49
	v_add_u32_e32 v51, v51, v48
	v_cmp_gt_u32_e64 s[46:47], 5, v47
	v_cmp_gt_u32_e64 s[48:49], 7, v48
	v_cmp_gt_u32_e32 vcc, 32, v51
	v_cmp_eq_u32_e64 s[50:51], 7, v48
	s_and_b64 s[46:47], s[46:47], s[48:49]
	s_and_b64 s[46:47], s[46:47], vcc
	v_min_u32_e32 v51, 31, v51
	v_lshl_add_u32 v51, v52, 5, v51
	v_lshlrev_b32_e32 v53, 2, v51
	global_load_dword v54, v53, s[26:27]
	v_lshl_add_u32 v55, v51, 2, v249
	s_mul_i32 s52, s52, 0x140
	s_mul_i32 s53, s36, 0x5000
	s_addk_i32 s53, 0x2800
	s_add_i32 s53, s53, s52
	s_add_u32 s42, s18, s53
	s_addc_u32 s43, s19, 0
	s_add_u32 s44, s42, 0x1400
	s_addc_u32 s45, s43, 0
	s_mov_b32 s81, 0x10000
	s_mov_b32 s82, 0x43800000
